# speedup vs baseline: 1.1512x; 1.1244x over previous
_Z12loss_combinePKfS0_Pf:
	s_load_dwordx4 s[4:7], s[0:1], 0x0
	s_load_dwordx2 s[2:3], s[0:1], 0x10
	v_lshlrev_b32_e32 v60, 4, v0
	v_lshlrev_b32_e32 v68, 2, v0
	v_mov_b32_e32 v3, 0
	s_mov_b32 s10, 0x800000
	s_mov_b32 s11, 0x3f317217
	s_mov_b32 s12, 0x7f800000
	v_mov_b32_e32 v2, 0x41b17218
	v_add_u32_e32 v61, 0x4000, v60
	v_add_u32_e32 v69, 0x1000, v68
	v_add_u32_e32 v62, 0x8000, v60
	v_add_u32_e32 v70, 0x2000, v68
	v_add_u32_e32 v63, 0xc000, v60
	v_add_u32_e32 v71, 0x3000, v68
	v_add_u32_e32 v64, 0x10000, v60
	v_add_u32_e32 v72, 0x4000, v68
	v_add_u32_e32 v65, 0x14000, v60
	v_add_u32_e32 v73, 0x5000, v68
	v_add_u32_e32 v66, 0x18000, v60
	v_add_u32_e32 v74, 0x6000, v68
	v_add_u32_e32 v67, 0x1c000, v60
	v_add_u32_e32 v75, 0x7000, v68
	s_waitcnt lgkmcnt(0)
	global_load_dwordx4 v[20:23], v60, s[4:5]
	global_load_dword v52, v68, s[6:7]
	global_load_dwordx4 v[24:27], v61, s[4:5]
	global_load_dword v53, v69, s[6:7]
	global_load_dwordx4 v[28:31], v62, s[4:5]
	global_load_dword v54, v70, s[6:7]
	global_load_dwordx4 v[32:35], v63, s[4:5]
	global_load_dword v55, v71, s[6:7]
	global_load_dwordx4 v[36:39], v64, s[4:5]
	global_load_dword v56, v72, s[6:7]
	global_load_dwordx4 v[40:43], v65, s[4:5]
	global_load_dword v57, v73, s[6:7]
	global_load_dwordx4 v[44:47], v66, s[4:5]
	global_load_dword v58, v74, s[6:7]
	global_load_dwordx4 v[48:51], v67, s[4:5]
	global_load_dword v59, v75, s[6:7]
	s_waitcnt vmcnt(15)
	v_max_f32_e32 v12, v22, v22
	v_max_f32_e32 v13, v20, v20
	v_max_f32_e32 v15, v13, v12
	v_sub_f32_e32 v20, v20, v15
	v_sub_f32_e32 v22, v22, v15
	v_mul_f32_e32 v20, 0x3fb8aa3b, v20
	v_mul_f32_e32 v22, 0x3fb8aa3b, v22
	v_exp_f32_e32 v12, v20
	v_exp_f32_e32 v13, v22
	v_mov_b32_e32 v22, v21
	v_pk_mul_f32 v[20:21], v[22:23], v[12:13]
	s_nop 0
	v_add_f32_e32 v20, v20, v21
	v_cmp_gt_f32_e64 s[0:1], s10, v20
	s_nop 1
	v_cndmask_b32_e64 v21, 0, 32, s[0:1]
	v_ldexp_f32 v20, v20, v21
	v_log_f32_e32 v20, v20
	v_cndmask_b32_e64 v21, 0, v2, s[0:1]
	v_mul_f32_e32 v22, 0x3f317217, v20
	v_fma_f32 v22, v20, s11, -v22
	v_fmac_f32_e32 v22, 0x3377d1cf, v20
	v_fmac_f32_e32 v22, 0x3f317217, v20
	v_cmp_lt_f32_e64 vcc, |v20|, s12
	s_nop 1
	v_cndmask_b32_e32 v20, v20, v22, vcc
	v_sub_f32_e32 v20, v20, v21
	v_add_f32_e32 v20, v15, v20
	s_waitcnt vmcnt(14)
	v_sub_f32_e32 v20, v20, v52
	v_add_f32_e32 v3, v3, v20
	s_waitcnt vmcnt(13)
	v_max_f32_e32 v12, v26, v26
	v_max_f32_e32 v13, v24, v24
	v_max_f32_e32 v15, v13, v12
	v_sub_f32_e32 v24, v24, v15
	v_sub_f32_e32 v26, v26, v15
	v_mul_f32_e32 v24, 0x3fb8aa3b, v24
	v_mul_f32_e32 v26, 0x3fb8aa3b, v26
	v_exp_f32_e32 v12, v24
	v_exp_f32_e32 v13, v26
	v_mov_b32_e32 v26, v25
	v_pk_mul_f32 v[24:25], v[26:27], v[12:13]
	s_nop 0
	v_add_f32_e32 v24, v24, v25
	v_cmp_gt_f32_e64 s[0:1], s10, v24
	s_nop 1
	v_cndmask_b32_e64 v25, 0, 32, s[0:1]
	v_ldexp_f32 v24, v24, v25
	v_log_f32_e32 v24, v24
	v_cndmask_b32_e64 v25, 0, v2, s[0:1]
	v_mul_f32_e32 v26, 0x3f317217, v24
	v_fma_f32 v26, v24, s11, -v26
	v_fmac_f32_e32 v26, 0x3377d1cf, v24
	v_fmac_f32_e32 v26, 0x3f317217, v24
	v_cmp_lt_f32_e64 vcc, |v24|, s12
	s_nop 1
	v_cndmask_b32_e32 v24, v24, v26, vcc
	v_sub_f32_e32 v24, v24, v25
	v_add_f32_e32 v24, v15, v24
	s_waitcnt vmcnt(12)
	v_sub_f32_e32 v24, v24, v53
	v_add_f32_e32 v3, v3, v24
	s_waitcnt vmcnt(11)
	v_max_f32_e32 v12, v30, v30
	v_max_f32_e32 v13, v28, v28
	v_max_f32_e32 v15, v13, v12
	v_sub_f32_e32 v28, v28, v15
	v_sub_f32_e32 v30, v30, v15
	v_mul_f32_e32 v28, 0x3fb8aa3b, v28
	v_mul_f32_e32 v30, 0x3fb8aa3b, v30
	v_exp_f32_e32 v12, v28
	v_exp_f32_e32 v13, v30
	v_mov_b32_e32 v30, v29
	v_pk_mul_f32 v[28:29], v[30:31], v[12:13]
	s_nop 0
	v_add_f32_e32 v28, v28, v29
	v_cmp_gt_f32_e64 s[0:1], s10, v28
	s_nop 1
	v_cndmask_b32_e64 v29, 0, 32, s[0:1]
	v_ldexp_f32 v28, v28, v29
	v_log_f32_e32 v28, v28
	v_cndmask_b32_e64 v29, 0, v2, s[0:1]
	v_mul_f32_e32 v30, 0x3f317217, v28
	v_fma_f32 v30, v28, s11, -v30
	v_fmac_f32_e32 v30, 0x3377d1cf, v28
	v_fmac_f32_e32 v30, 0x3f317217, v28
	v_cmp_lt_f32_e64 vcc, |v28|, s12
	s_nop 1
	v_cndmask_b32_e32 v28, v28, v30, vcc
	v_sub_f32_e32 v28, v28, v29
	v_add_f32_e32 v28, v15, v28
	s_waitcnt vmcnt(10)
	v_sub_f32_e32 v28, v28, v54
	v_add_f32_e32 v3, v3, v28
	s_waitcnt vmcnt(9)
	v_max_f32_e32 v12, v34, v34
	v_max_f32_e32 v13, v32, v32
	v_max_f32_e32 v15, v13, v12
	v_sub_f32_e32 v32, v32, v15
	v_sub_f32_e32 v34, v34, v15
	v_mul_f32_e32 v32, 0x3fb8aa3b, v32
	v_mul_f32_e32 v34, 0x3fb8aa3b, v34
	v_exp_f32_e32 v12, v32
	v_exp_f32_e32 v13, v34
	v_mov_b32_e32 v34, v33
	v_pk_mul_f32 v[32:33], v[34:35], v[12:13]
	s_nop 0
	v_add_f32_e32 v32, v32, v33
	v_cmp_gt_f32_e64 s[0:1], s10, v32
	s_nop 1
	v_cndmask_b32_e64 v33, 0, 32, s[0:1]
	v_ldexp_f32 v32, v32, v33
	v_log_f32_e32 v32, v32
	v_cndmask_b32_e64 v33, 0, v2, s[0:1]
	v_mul_f32_e32 v34, 0x3f317217, v32
	v_fma_f32 v34, v32, s11, -v34
	v_fmac_f32_e32 v34, 0x3377d1cf, v32
	v_fmac_f32_e32 v34, 0x3f317217, v32
	v_cmp_lt_f32_e64 vcc, |v32|, s12
	s_nop 1
	v_cndmask_b32_e32 v32, v32, v34, vcc
	v_sub_f32_e32 v32, v32, v33
	v_add_f32_e32 v32, v15, v32
	s_waitcnt vmcnt(8)
	v_sub_f32_e32 v32, v32, v55
	v_add_f32_e32 v3, v3, v32
	s_waitcnt vmcnt(7)
	v_max_f32_e32 v12, v38, v38
	v_max_f32_e32 v13, v36, v36
	v_max_f32_e32 v15, v13, v12
	v_sub_f32_e32 v36, v36, v15
	v_sub_f32_e32 v38, v38, v15
	v_mul_f32_e32 v36, 0x3fb8aa3b, v36
	v_mul_f32_e32 v38, 0x3fb8aa3b, v38
	v_exp_f32_e32 v12, v36
	v_exp_f32_e32 v13, v38
	v_mov_b32_e32 v38, v37
	v_pk_mul_f32 v[36:37], v[38:39], v[12:13]
	s_nop 0
	v_add_f32_e32 v36, v36, v37
	v_cmp_gt_f32_e64 s[0:1], s10, v36
	s_nop 1
	v_cndmask_b32_e64 v37, 0, 32, s[0:1]
	v_ldexp_f32 v36, v36, v37
	v_log_f32_e32 v36, v36
	v_cndmask_b32_e64 v37, 0, v2, s[0:1]
	v_mul_f32_e32 v38, 0x3f317217, v36
	v_fma_f32 v38, v36, s11, -v38
	v_fmac_f32_e32 v38, 0x3377d1cf, v36
	v_fmac_f32_e32 v38, 0x3f317217, v36
	v_cmp_lt_f32_e64 vcc, |v36|, s12
	s_nop 1
	v_cndmask_b32_e32 v36, v36, v38, vcc
	v_sub_f32_e32 v36, v36, v37
	v_add_f32_e32 v36, v15, v36
	s_waitcnt vmcnt(6)
	v_sub_f32_e32 v36, v36, v56
	v_add_f32_e32 v3, v3, v36
	s_waitcnt vmcnt(5)
	v_max_f32_e32 v12, v42, v42
	v_max_f32_e32 v13, v40, v40
	v_max_f32_e32 v15, v13, v12
	v_sub_f32_e32 v40, v40, v15
	v_sub_f32_e32 v42, v42, v15
	v_mul_f32_e32 v40, 0x3fb8aa3b, v40
	v_mul_f32_e32 v42, 0x3fb8aa3b, v42
	v_exp_f32_e32 v12, v40
	v_exp_f32_e32 v13, v42
	v_mov_b32_e32 v42, v41
	v_pk_mul_f32 v[40:41], v[42:43], v[12:13]
	s_nop 0
	v_add_f32_e32 v40, v40, v41
	v_cmp_gt_f32_e64 s[0:1], s10, v40
	s_nop 1
	v_cndmask_b32_e64 v41, 0, 32, s[0:1]
	v_ldexp_f32 v40, v40, v41
	v_log_f32_e32 v40, v40
	v_cndmask_b32_e64 v41, 0, v2, s[0:1]
	v_mul_f32_e32 v42, 0x3f317217, v40
	v_fma_f32 v42, v40, s11, -v42
	v_fmac_f32_e32 v42, 0x3377d1cf, v40
	v_fmac_f32_e32 v42, 0x3f317217, v40
	v_cmp_lt_f32_e64 vcc, |v40|, s12
	s_nop 1
	v_cndmask_b32_e32 v40, v40, v42, vcc
	v_sub_f32_e32 v40, v40, v41
	v_add_f32_e32 v40, v15, v40
	s_waitcnt vmcnt(4)
	v_sub_f32_e32 v40, v40, v57
	v_add_f32_e32 v3, v3, v40
	s_waitcnt vmcnt(3)
	v_max_f32_e32 v12, v46, v46
	v_max_f32_e32 v13, v44, v44
	v_max_f32_e32 v15, v13, v12
	v_sub_f32_e32 v44, v44, v15
	v_sub_f32_e32 v46, v46, v15
	v_mul_f32_e32 v44, 0x3fb8aa3b, v44
	v_mul_f32_e32 v46, 0x3fb8aa3b, v46
	v_exp_f32_e32 v12, v44
	v_exp_f32_e32 v13, v46
	v_mov_b32_e32 v46, v45
	v_pk_mul_f32 v[44:45], v[46:47], v[12:13]
	s_nop 0
	v_add_f32_e32 v44, v44, v45
	v_cmp_gt_f32_e64 s[0:1], s10, v44
	s_nop 1
	v_cndmask_b32_e64 v45, 0, 32, s[0:1]
	v_ldexp_f32 v44, v44, v45
	v_log_f32_e32 v44, v44
	v_cndmask_b32_e64 v45, 0, v2, s[0:1]
	v_mul_f32_e32 v46, 0x3f317217, v44
	v_fma_f32 v46, v44, s11, -v46
	v_fmac_f32_e32 v46, 0x3377d1cf, v44
	v_fmac_f32_e32 v46, 0x3f317217, v44
	v_cmp_lt_f32_e64 vcc, |v44|, s12
	s_nop 1
	v_cndmask_b32_e32 v44, v44, v46, vcc
	v_sub_f32_e32 v44, v44, v45
	v_add_f32_e32 v44, v15, v44
	s_waitcnt vmcnt(2)
	v_sub_f32_e32 v44, v44, v58
	v_add_f32_e32 v3, v3, v44
	s_waitcnt vmcnt(1)
	v_max_f32_e32 v12, v50, v50
	v_max_f32_e32 v13, v48, v48
	v_max_f32_e32 v15, v13, v12
	v_sub_f32_e32 v48, v48, v15
	v_sub_f32_e32 v50, v50, v15
	v_mul_f32_e32 v48, 0x3fb8aa3b, v48
	v_mul_f32_e32 v50, 0x3fb8aa3b, v50
	v_exp_f32_e32 v12, v48
	v_exp_f32_e32 v13, v50
	v_mov_b32_e32 v50, v49
	v_pk_mul_f32 v[48:49], v[50:51], v[12:13]
	s_nop 0
	v_add_f32_e32 v48, v48, v49
	v_cmp_gt_f32_e64 s[0:1], s10, v48
	s_nop 1
	v_cndmask_b32_e64 v49, 0, 32, s[0:1]
	v_ldexp_f32 v48, v48, v49
	v_log_f32_e32 v48, v48
	v_cndmask_b32_e64 v49, 0, v2, s[0:1]
	v_mul_f32_e32 v50, 0x3f317217, v48
	v_fma_f32 v50, v48, s11, -v50
	v_fmac_f32_e32 v50, 0x3377d1cf, v48
	v_fmac_f32_e32 v50, 0x3f317217, v48
	v_cmp_lt_f32_e64 vcc, |v48|, s12
	s_nop 1
	v_cndmask_b32_e32 v48, v48, v50, vcc
	v_sub_f32_e32 v48, v48, v49
	v_add_f32_e32 v48, v15, v48
	s_waitcnt vmcnt(0)
	v_sub_f32_e32 v48, v48, v59
	v_add_f32_e32 v3, v3, v48
	v_mbcnt_lo_u32_b32 v1, -1, 0
	v_mbcnt_hi_u32_b32 v2, -1, v1
	v_and_b32_e32 v1, 64, v2
	v_add_u32_e32 v4, 64, v1
	v_xor_b32_e32 v1, 32, v2
	v_cmp_lt_i32_e32 vcc, v1, v4
	v_xor_b32_e32 v5, 16, v2
	s_nop 0
	v_cndmask_b32_e32 v1, v2, v1, vcc
	v_lshlrev_b32_e32 v1, 2, v1
	ds_bpermute_b32 v1, v1, v3
	v_cmp_lt_i32_e32 vcc, v5, v4
	s_waitcnt lgkmcnt(0)
	v_add_f32_e32 v1, v3, v1
	v_cndmask_b32_e32 v3, v2, v5, vcc
	v_lshlrev_b32_e32 v3, 2, v3
	ds_bpermute_b32 v3, v3, v1
	v_xor_b32_e32 v5, 8, v2
	v_cmp_lt_i32_e32 vcc, v5, v4
	s_waitcnt lgkmcnt(0)
	v_add_f32_e32 v1, v1, v3
	v_cndmask_b32_e32 v3, v2, v5, vcc
	v_lshlrev_b32_e32 v3, 2, v3
	ds_bpermute_b32 v3, v3, v1
	v_xor_b32_e32 v5, 4, v2
	v_cmp_lt_i32_e32 vcc, v5, v4
	s_waitcnt lgkmcnt(0)
	v_add_f32_e32 v1, v1, v3
	v_cndmask_b32_e32 v3, v2, v5, vcc
	v_lshlrev_b32_e32 v3, 2, v3
	ds_bpermute_b32 v3, v3, v1
	v_xor_b32_e32 v5, 2, v2
	v_cmp_lt_i32_e32 vcc, v5, v4
	s_waitcnt lgkmcnt(0)
	v_add_f32_e32 v1, v1, v3
	v_cndmask_b32_e32 v3, v2, v5, vcc
	v_lshlrev_b32_e32 v3, 2, v3
	ds_bpermute_b32 v3, v3, v1
	v_xor_b32_e32 v5, 1, v2
	v_cmp_lt_i32_e32 vcc, v5, v4
	s_waitcnt lgkmcnt(0)
	v_add_f32_e32 v1, v1, v3
	v_cndmask_b32_e32 v2, v2, v5, vcc
	v_lshlrev_b32_e32 v2, 2, v2
	ds_bpermute_b32 v2, v2, v1
	v_and_b32_e32 v3, 63, v0
	v_cmp_eq_u32_e32 vcc, 0, v3
	s_and_saveexec_b64 s[0:1], vcc
	s_cbranch_execz .LBB3_4
	v_lshrrev_b32_e32 v3, 4, v0
	s_waitcnt lgkmcnt(0)
	v_add_f32_e32 v1, v1, v2
	ds_write_b32 v3, v1

	.amdhsa_kernel _Z12loss_combinePKfS0_Pf
		.amdhsa_group_segment_fixed_size 64
		.amdhsa_private_segment_fixed_size 0
		.amdhsa_kernarg_size 24
		.amdhsa_user_sgpr_count 2
		.amdhsa_user_sgpr_dispatch_ptr 0
		.amdhsa_user_sgpr_queue_ptr 0
		.amdhsa_user_sgpr_kernarg_segment_ptr 1
		.amdhsa_user_sgpr_dispatch_id 0
		.amdhsa_user_sgpr_kernarg_preload_length 0
		.amdhsa_user_sgpr_kernarg_preload_offset 0
		.amdhsa_user_sgpr_private_segment_size 0
		.amdhsa_uses_dynamic_stack 0
		.amdhsa_enable_private_segment 0
		.amdhsa_system_sgpr_workgroup_id_x 1
		.amdhsa_system_sgpr_workgroup_id_y 0
		.amdhsa_system_sgpr_workgroup_id_z 0
		.amdhsa_system_sgpr_workgroup_info 0
		.amdhsa_system_vgpr_workitem_id 0
		.amdhsa_next_free_vgpr 76
		.amdhsa_next_free_sgpr 14
		.amdhsa_accum_offset 76
		.amdhsa_reserve_vcc 1
		.amdhsa_float_round_mode_32 0
		.amdhsa_float_round_mode_16_64 0
		.amdhsa_float_denorm_mode_32 3
		.amdhsa_float_denorm_mode_16_64 3
		.amdhsa_dx10_clamp 1
		.amdhsa_ieee_mode 1
		.amdhsa_fp16_overflow 0
		.amdhsa_tg_split 0
		.amdhsa_exception_fp_ieee_invalid_op 0
		.amdhsa_exception_fp_denorm_src 0
		.amdhsa_exception_fp_ieee_div_zero 0
		.amdhsa_exception_fp_ieee_overflow 0
		.amdhsa_exception_fp_ieee_underflow 0
		.amdhsa_exception_fp_ieee_inexact 0
		.amdhsa_exception_int_div_zero 0
	.end_amdhsa_kernel

.LBB10_5:
	s_or_b64 exec, exec, s[12:13]
	s_mul_i32 s7, s7, s30
	s_sub_i32 s12, s33, s7
	s_lshl_b32 s22, s12, 7
	s_ashr_i32 s23, s22, 31
	s_lshl_b64 s[28:29], s[22:23], 2
	s_waitcnt lgkmcnt(0)
	s_barrier
	v_lshl_add_u64 v[10:11], v[68:69], 0, s[28:29]
	global_load_dwordx4 v[6:9], v[10:11], off
	global_load_dwordx4 v[2:5], v[10:11], off offset:16
	v_lshl_add_u64 v[18:19], v[70:71], 0, s[28:29]
	global_load_dwordx4 v[14:17], v[18:19], off
	global_load_dwordx4 v[10:13], v[18:19], off offset:16
	v_and_b32_e32 v18, 64, v114
	v_add_u32_e32 v19, 0, v87
	v_add_u32_e32 v22, s5, v87
	v_add_u32_e32 v26, 0, v88
	v_add_u32_e32 v27, s5, v88
	v_add_u32_e32 v44, 64, v18
	ds_read_b128 v[18:21], v19
	ds_read_b128 v[22:25], v22
	ds_read_b128 v[34:37], v26
	ds_read_b128 v[38:41], v27
	s_waitcnt vmcnt(4)
	ds_read_b64 v[26:27], v89
	v_xor_b32_e32 v30, 8, v114
	v_or_b32_e32 v28, s6, v66
	v_xor_b32_e32 v31, 4, v114
	v_cmp_lt_i32_e64 s[2:3], v30, v44
	v_ashrrev_i32_e32 v29, 31, v28
	s_waitcnt lgkmcnt(3)
	v_pk_add_f32 v[20:21], v[20:21], v[24:25]
	v_cndmask_b32_e64 v30, v114, v30, s[2:3]
	v_cmp_lt_i32_e64 s[2:3], v31, v44
	v_pk_add_f32 v[18:19], v[18:19], v[22:23]
	s_waitcnt lgkmcnt(1)
	v_pk_add_f32 v[22:23], v[36:37], v[40:41]
	v_pk_add_f32 v[24:25], v[34:35], v[38:39]
	v_lshl_add_u64 v[42:43], v[28:29], 2, s[26:27]
	v_cndmask_b32_e64 v45, v114, v31, s[2:3]
	v_lshlrev_b32_e32 v33, 2, v30
	v_lshlrev_b32_e32 v34, 2, v45
	s_waitcnt vmcnt(3) lgkmcnt(0)
	v_pk_fma_f32 v[18:19], v[26:27], v[6:7], v[18:19] op_sel_hi:[0,1,1] neg_lo:[1,0,0] neg_hi:[1,0,0]
	s_waitcnt vmcnt(2)
	v_pk_fma_f32 v[24:25], v[26:27], v[2:3], v[24:25] op_sel_hi:[0,1,1] neg_lo:[1,0,0] neg_hi:[1,0,0]
	v_pk_fma_f32 v[20:21], v[26:27], v[8:9], v[20:21] op_sel_hi:[0,1,1] neg_lo:[1,0,0] neg_hi:[1,0,0]
	v_pk_fma_f32 v[30:31], v[26:27], v[4:5], v[22:23] op_sel_hi:[0,1,1] neg_lo:[1,0,0] neg_hi:[1,0,0]
	s_waitcnt vmcnt(1)
	v_pk_fma_f32 v[22:23], v[26:27], v[18:19], v[14:15] op_sel:[1,0,0]
	s_waitcnt vmcnt(0)
	v_pk_fma_f32 v[18:19], v[26:27], v[24:25], v[10:11] op_sel:[1,0,0]
	v_pk_fma_f32 v[24:25], v[26:27], v[20:21], v[16:17] op_sel:[1,0,0]
	v_pk_fma_f32 v[20:21], v[26:27], v[30:31], v[12:13] op_sel:[1,0,0]
	global_load_dword v31, v[42:43], off
	global_load_dword v39, v[42:43], off offset:128
	global_load_dword v38, v[42:43], off offset:256
	global_load_dword v32, v[42:43], off offset:384
	v_max_f32_e32 v30, v20, v21
	v_max_f32_e32 v26, v22, v23
	v_max_f32_e32 v27, v24, v25
	v_max3_f32 v30, v18, v19, v30
	v_max3_f32 v26, v26, v27, v30
	s_nop 1
	v_mov_b32_dpp v27, v26 row_mirror row_mask:0xf bank_mask:0xf
	v_xor_b32_e32 v30, 2, v114
	v_cmp_lt_i32_e64 s[2:3], v30, v44
	s_waitcnt lgkmcnt(0)
	v_max_f32_e32 v27, v27, v27
	v_max_f32_e32 v26, v26, v27
	s_nop 1
	v_mov_b32_dpp v27, v26 row_half_mirror row_mask:0xf bank_mask:0xf
	v_cndmask_b32_e64 v30, v114, v30, s[2:3]
	v_lshlrev_b32_e32 v35, 2, v30
	v_xor_b32_e32 v30, 1, v114
	v_cmp_lt_i32_e64 s[2:3], v30, v44
	s_waitcnt lgkmcnt(0)
	v_max_f32_e32 v27, v27, v27
	v_max_f32_e32 v26, v26, v27
	s_nop 1
	v_mov_b32_dpp v27, v26 quad_perm:[2,3,0,1] row_mask:0xf bank_mask:0xf
	v_cndmask_b32_e64 v30, v114, v30, s[2:3]
	v_lshlrev_b32_e32 v36, 2, v30
	s_waitcnt lgkmcnt(0)
	v_max_f32_e32 v27, v27, v27
	v_max_f32_e32 v26, v26, v27
	s_nop 1
	v_mov_b32_dpp v27, v26 quad_perm:[1,0,3,2] row_mask:0xf bank_mask:0xf
	s_waitcnt lgkmcnt(0)
	v_max_f32_e32 v27, v27, v27
	v_max_f32_e32 v30, v26, v27
	v_sub_f32_e32 v26, v22, v30
	v_sub_f32_e32 v27, v18, v30
	v_sub_f32_e32 v37, v23, v30
	v_sub_f32_e32 v40, v19, v30
	v_mul_f32_e32 v26, 0x3fb8aa3b, v26
	v_mul_f32_e32 v27, 0x3fb8aa3b, v27
	v_sub_f32_e32 v41, v24, v30
	v_sub_f32_e32 v42, v20, v30
	v_mul_f32_e32 v37, 0x3fb8aa3b, v37
	v_mul_f32_e32 v40, 0x3fb8aa3b, v40
	v_exp_f32_e32 v26, v26
	v_exp_f32_e32 v27, v27
	v_sub_f32_e32 v43, v25, v30
	v_sub_f32_e32 v44, v21, v30
	v_mul_f32_e32 v41, 0x3fb8aa3b, v41
	v_mul_f32_e32 v42, 0x3fb8aa3b, v42
	v_exp_f32_e32 v37, v37
	v_exp_f32_e32 v40, v40
	v_mul_f32_e32 v43, 0x3fb8aa3b, v43
	v_mul_f32_e32 v44, 0x3fb8aa3b, v44
	v_exp_f32_e32 v41, v41
	v_exp_f32_e32 v42, v42
	v_exp_f32_e32 v43, v43
	v_exp_f32_e32 v44, v44
	v_add_f32_e32 v26, v26, v27
	v_add_f32_e32 v27, v37, v40
	v_add_f32_e32 v26, 0, v26
	v_add_f32_e32 v37, v41, v42
	v_add_f32_e32 v26, v26, v27
	v_add_f32_e32 v26, v26, v37
	v_add_f32_e32 v27, v43, v44
	v_add_f32_e32 v26, v26, v27
	s_nop 1
	v_mov_b32_dpp v27, v26 row_mirror row_mask:0xf bank_mask:0xf
	s_waitcnt lgkmcnt(0)
	v_add_f32_e32 v37, v26, v27
	s_nop 1
	v_mov_b32_dpp v40, v37 row_half_mirror row_mask:0xf bank_mask:0xf
	v_lshl_add_u64 v[26:27], v[72:73], 0, s[28:29]
	s_waitcnt lgkmcnt(0)
	v_add_f32_e32 v44, v37, v40
	s_nop 1
	v_mov_b32_dpp v45, v44 quad_perm:[2,3,0,1] row_mask:0xf bank_mask:0xf
	v_mad_i64_i32 v[40:41], s[2:3], v28, s14, 0
	v_lshl_add_u64 v[42:43], v[40:41], 2, v[26:27]
	v_or_b32_e32 v37, s22, v80
	s_waitcnt lgkmcnt(0)
	v_add_f32_e32 v40, v44, v45
	s_nop 1
	v_mov_b32_dpp v41, v40 quad_perm:[1,0,3,2] row_mask:0xf bank_mask:0xf
	global_store_dwordx4 v[42:43], v[22:25], off
	global_store_dwordx4 v[42:43], v[18:21], off offset:16
	s_waitcnt vmcnt(5)
	v_sub_u32_e32 v42, v31, v37
	v_cmp_gt_u32_e64 s[2:3], 8, v42
	s_and_saveexec_b64 s[22:23], s[2:3]
	s_cbranch_execz .LBB10_7
	v_cmp_eq_u32_e64 s[2:3], v31, v37
	s_nop 1
	v_cndmask_b32_e64 v22, 0, v22, s[2:3]
	v_cmp_eq_u32_e64 s[2:3], 4, v42
	s_nop 1
	v_cndmask_b32_e64 v18, v22, v18, s[2:3]
	v_cmp_eq_u32_e64 s[2:3], 1, v42
	s_nop 1
	v_cndmask_b32_e64 v18, v18, v23, s[2:3]
	v_cmp_eq_u32_e64 s[2:3], 5, v42
	s_nop 1
	v_cndmask_b32_e64 v18, v18, v19, s[2:3]
	v_cmp_eq_u32_e64 s[2:3], 2, v42
	s_nop 1
	v_cndmask_b32_e64 v18, v18, v24, s[2:3]
	v_cmp_eq_u32_e64 s[2:3], 6, v42
	s_nop 1
	v_cndmask_b32_e64 v18, v18, v20, s[2:3]
	v_cmp_eq_u32_e64 s[2:3], 3, v42
	s_nop 1
	v_cndmask_b32_e64 v18, v18, v25, s[2:3]
	v_cmp_eq_u32_e64 s[2:3], 7, v42
	s_nop 1
	v_cndmask_b32_e64 v20, v18, v21, s[2:3]
	v_lshl_add_u64 v[18:19], v[28:29], 2, s[24:25]
	global_store_dword v[18:19], v20, off

.LBB10_9:
	s_or_b64 exec, exec, s[2:3]
	v_add_u32_e32 v18, 0, v91
	v_add_u32_e32 v22, s5, v91
	v_add_u32_e32 v28, 0, v92
	v_add_u32_e32 v40, s5, v92
	ds_read_b128 v[18:21], v18
	ds_read_b128 v[22:25], v22
	ds_read_b128 v[28:31], v28
	ds_read_b64 v[44:45], v93
	s_waitcnt lgkmcnt(4)
	ds_read_b128 v[40:43], v40
	s_waitcnt lgkmcnt(3)
	v_pk_add_f32 v[20:21], v[20:21], v[24:25]
	v_pk_add_f32 v[18:19], v[18:19], v[22:23]
	s_waitcnt lgkmcnt(0)
	v_pk_add_f32 v[24:25], v[30:31], v[42:43]
	v_pk_add_f32 v[22:23], v[28:29], v[40:41]
	v_pk_fma_f32 v[24:25], v[44:45], v[4:5], v[24:25] op_sel_hi:[0,1,1] neg_lo:[1,0,0] neg_hi:[1,0,0]
	v_pk_fma_f32 v[18:19], v[44:45], v[6:7], v[18:19] op_sel_hi:[0,1,1] neg_lo:[1,0,0] neg_hi:[1,0,0]
	v_pk_fma_f32 v[22:23], v[44:45], v[2:3], v[22:23] op_sel_hi:[0,1,1] neg_lo:[1,0,0] neg_hi:[1,0,0]
	v_pk_fma_f32 v[20:21], v[44:45], v[8:9], v[20:21] op_sel_hi:[0,1,1] neg_lo:[1,0,0] neg_hi:[1,0,0]
	v_pk_fma_f32 v[24:25], v[44:45], v[24:25], v[12:13] op_sel:[1,0,0]
	v_pk_fma_f32 v[18:19], v[44:45], v[18:19], v[14:15] op_sel:[1,0,0]
	v_pk_fma_f32 v[22:23], v[44:45], v[22:23], v[10:11] op_sel:[1,0,0]
	v_pk_fma_f32 v[20:21], v[44:45], v[20:21], v[16:17] op_sel:[1,0,0]
	v_max_f32_e32 v30, v24, v25
	v_max_f32_e32 v28, v18, v19
	v_max_f32_e32 v29, v20, v21
	v_max3_f32 v30, v22, v23, v30
	v_max3_f32 v28, v28, v29, v30
	s_nop 1
	v_mov_b32_dpp v29, v28 row_mirror row_mask:0xf bank_mask:0xf
	s_waitcnt lgkmcnt(0)
	v_max_f32_e32 v29, v29, v29
	v_max_f32_e32 v28, v28, v29
	s_nop 1
	v_mov_b32_dpp v29, v28 row_half_mirror row_mask:0xf bank_mask:0xf
	s_waitcnt lgkmcnt(0)
	v_max_f32_e32 v29, v29, v29
	v_max_f32_e32 v28, v28, v29
	s_nop 1
	v_mov_b32_dpp v29, v28 quad_perm:[2,3,0,1] row_mask:0xf bank_mask:0xf
	s_waitcnt lgkmcnt(0)
	v_max_f32_e32 v29, v29, v29
	v_max_f32_e32 v28, v28, v29
	s_nop 1
	v_mov_b32_dpp v29, v28 quad_perm:[1,0,3,2] row_mask:0xf bank_mask:0xf
	s_waitcnt lgkmcnt(0)
	v_max_f32_e32 v29, v29, v29
	v_max_f32_e32 v28, v28, v29
	v_sub_f32_e32 v29, v18, v28
	v_sub_f32_e32 v30, v22, v28
	v_sub_f32_e32 v31, v19, v28
	v_sub_f32_e32 v40, v23, v28
	v_mul_f32_e32 v29, 0x3fb8aa3b, v29
	v_mul_f32_e32 v30, 0x3fb8aa3b, v30
	v_mul_f32_e32 v31, 0x3fb8aa3b, v31
	v_mul_f32_e32 v40, 0x3fb8aa3b, v40
	v_exp_f32_e32 v29, v29
	v_exp_f32_e32 v30, v30
	v_exp_f32_e32 v31, v31
	v_exp_f32_e32 v40, v40
	v_sub_f32_e32 v41, v21, v28
	v_add_f32_e32 v29, v29, v30
	v_sub_f32_e32 v42, v25, v28
	v_add_f32_e32 v30, v31, v40
	v_sub_f32_e32 v31, v20, v28
	v_sub_f32_e32 v40, v24, v28
	v_mul_f32_e32 v31, 0x3fb8aa3b, v31
	v_mul_f32_e32 v40, 0x3fb8aa3b, v40
	v_exp_f32_e32 v31, v31
	v_exp_f32_e32 v40, v40
	v_mul_f32_e32 v41, 0x3fb8aa3b, v41
	v_mul_f32_e32 v42, 0x3fb8aa3b, v42
	v_exp_f32_e32 v41, v41
	v_exp_f32_e32 v42, v42
	v_add_f32_e32 v29, 0, v29
	v_add_f32_e32 v29, v29, v30
	v_add_f32_e32 v30, v31, v40
	v_add_f32_e32 v29, v29, v30
	v_add_f32_e32 v30, v41, v42
	v_add_f32_e32 v29, v29, v30
	s_nop 1
	v_mov_b32_dpp v30, v29 row_mirror row_mask:0xf bank_mask:0xf
	s_waitcnt lgkmcnt(0)
	v_add_f32_e32 v29, v29, v30
	s_nop 1
	v_mov_b32_dpp v30, v29 row_half_mirror row_mask:0xf bank_mask:0xf
	s_waitcnt lgkmcnt(0)
	v_add_f32_e32 v29, v29, v30
	s_nop 1
	v_mov_b32_dpp v31, v29 quad_perm:[2,3,0,1] row_mask:0xf bank_mask:0xf
	v_or_b32_e32 v30, s6, v90
	v_mad_i64_i32 v[40:41], s[2:3], v30, s14, 0
	v_lshl_add_u64 v[42:43], v[40:41], 2, v[26:27]
	s_waitcnt lgkmcnt(0)
	v_add_f32_e32 v29, v29, v31
	s_nop 1
	v_mov_b32_dpp v40, v29 quad_perm:[1,0,3,2] row_mask:0xf bank_mask:0xf
	s_waitcnt vmcnt(4)
	v_sub_u32_e32 v31, v39, v37
	v_cmp_gt_u32_e64 s[2:3], 8, v31
	global_store_dwordx4 v[42:43], v[18:21], off
	global_store_dwordx4 v[42:43], v[22:25], off offset:16
	s_and_saveexec_b64 s[22:23], s[2:3]
	s_cbranch_execz .LBB10_11
	v_cmp_eq_u32_e64 s[2:3], v39, v37
	s_ashr_i32 s7, s6, 31
	s_nop 0
	v_cndmask_b32_e64 v18, 0, v18, s[2:3]
	v_cmp_eq_u32_e64 s[2:3], 4, v31
	s_nop 1
	v_cndmask_b32_e64 v18, v18, v22, s[2:3]
	v_cmp_eq_u32_e64 s[2:3], 1, v31
	s_nop 1
	v_cndmask_b32_e64 v18, v18, v19, s[2:3]
	v_cmp_eq_u32_e64 s[2:3], 5, v31
	s_nop 1
	v_cndmask_b32_e64 v18, v18, v23, s[2:3]
	v_cmp_eq_u32_e64 s[2:3], 2, v31
	s_nop 1
	v_cndmask_b32_e64 v18, v18, v20, s[2:3]
	v_cmp_eq_u32_e64 s[2:3], 6, v31
	s_nop 1
	v_cndmask_b32_e64 v18, v18, v24, s[2:3]
	v_cmp_eq_u32_e64 s[2:3], 3, v31
	s_nop 1
	v_cndmask_b32_e64 v18, v18, v21, s[2:3]
	v_cmp_eq_u32_e64 s[2:3], 7, v31
	s_nop 1
	v_cndmask_b32_e64 v20, v18, v25, s[2:3]
	v_lshl_add_u64 v[18:19], v[66:67], 0, s[6:7]
	v_lshl_add_u64 v[18:19], v[18:19], 2, s[24:25]
	global_store_dword v[18:19], v20, off offset:128

.LBB10_13:
	s_or_b64 exec, exec, s[2:3]
	v_add_u32_e32 v18, 0, v95
	v_add_u32_e32 v22, s5, v95
	v_add_u32_e32 v28, 0, v96
	v_add_u32_e32 v39, s5, v96
	ds_read_b128 v[18:21], v18
	ds_read_b128 v[22:25], v22
	ds_read_b128 v[28:31], v28
	ds_read_b64 v[44:45], v97
	s_waitcnt lgkmcnt(4)
	ds_read_b128 v[40:43], v39
	s_waitcnt lgkmcnt(3)
	v_pk_add_f32 v[20:21], v[20:21], v[24:25]
	v_pk_add_f32 v[18:19], v[18:19], v[22:23]
	s_waitcnt lgkmcnt(0)
	v_pk_add_f32 v[24:25], v[30:31], v[42:43]
	v_pk_add_f32 v[22:23], v[28:29], v[40:41]
	v_pk_fma_f32 v[24:25], v[44:45], v[4:5], v[24:25] op_sel_hi:[0,1,1] neg_lo:[1,0,0] neg_hi:[1,0,0]
	v_pk_fma_f32 v[18:19], v[44:45], v[6:7], v[18:19] op_sel_hi:[0,1,1] neg_lo:[1,0,0] neg_hi:[1,0,0]
	v_pk_fma_f32 v[22:23], v[44:45], v[2:3], v[22:23] op_sel_hi:[0,1,1] neg_lo:[1,0,0] neg_hi:[1,0,0]
	v_pk_fma_f32 v[20:21], v[44:45], v[8:9], v[20:21] op_sel_hi:[0,1,1] neg_lo:[1,0,0] neg_hi:[1,0,0]
	v_pk_fma_f32 v[24:25], v[44:45], v[24:25], v[12:13] op_sel:[1,0,0]
	v_pk_fma_f32 v[18:19], v[44:45], v[18:19], v[14:15] op_sel:[1,0,0]
	v_pk_fma_f32 v[22:23], v[44:45], v[22:23], v[10:11] op_sel:[1,0,0]
	v_pk_fma_f32 v[20:21], v[44:45], v[20:21], v[16:17] op_sel:[1,0,0]
	v_max_f32_e32 v30, v24, v25
	v_max_f32_e32 v28, v18, v19
	v_max_f32_e32 v29, v20, v21
	v_max3_f32 v30, v22, v23, v30
	v_max3_f32 v28, v28, v29, v30
	s_nop 1
	v_mov_b32_dpp v29, v28 row_mirror row_mask:0xf bank_mask:0xf
	s_waitcnt lgkmcnt(0)
	v_max_f32_e32 v29, v29, v29
	v_max_f32_e32 v28, v28, v29
	s_nop 1
	v_mov_b32_dpp v29, v28 row_half_mirror row_mask:0xf bank_mask:0xf
	s_waitcnt lgkmcnt(0)
	v_max_f32_e32 v29, v29, v29
	v_max_f32_e32 v28, v28, v29
	s_nop 1
	v_mov_b32_dpp v29, v28 quad_perm:[2,3,0,1] row_mask:0xf bank_mask:0xf
	s_waitcnt lgkmcnt(0)
	v_max_f32_e32 v29, v29, v29
	v_max_f32_e32 v28, v28, v29
	s_nop 1
	v_mov_b32_dpp v29, v28 quad_perm:[1,0,3,2] row_mask:0xf bank_mask:0xf
	s_waitcnt lgkmcnt(0)
	v_max_f32_e32 v29, v29, v29
	v_max_f32_e32 v28, v28, v29
	v_sub_f32_e32 v29, v18, v28
	v_sub_f32_e32 v30, v22, v28
	v_sub_f32_e32 v31, v19, v28
	v_sub_f32_e32 v39, v23, v28
	v_mul_f32_e32 v29, 0x3fb8aa3b, v29
	v_mul_f32_e32 v30, 0x3fb8aa3b, v30
	v_mul_f32_e32 v31, 0x3fb8aa3b, v31
	v_mul_f32_e32 v39, 0x3fb8aa3b, v39
	v_exp_f32_e32 v29, v29
	v_exp_f32_e32 v30, v30
	v_exp_f32_e32 v31, v31
	v_exp_f32_e32 v39, v39
	v_sub_f32_e32 v40, v21, v28
	v_add_f32_e32 v29, v29, v30
	v_sub_f32_e32 v41, v25, v28
	v_add_f32_e32 v30, v31, v39
	v_sub_f32_e32 v31, v20, v28
	v_sub_f32_e32 v39, v24, v28
	v_mul_f32_e32 v31, 0x3fb8aa3b, v31
	v_mul_f32_e32 v39, 0x3fb8aa3b, v39
	v_exp_f32_e32 v31, v31
	v_exp_f32_e32 v39, v39
	v_mul_f32_e32 v40, 0x3fb8aa3b, v40
	v_mul_f32_e32 v41, 0x3fb8aa3b, v41
	v_exp_f32_e32 v40, v40
	v_exp_f32_e32 v41, v41
	v_add_f32_e32 v29, 0, v29
	v_add_f32_e32 v29, v29, v30
	v_add_f32_e32 v30, v31, v39
	v_add_f32_e32 v29, v29, v30
	v_add_f32_e32 v30, v40, v41
	v_add_f32_e32 v29, v29, v30
	s_nop 1
	v_mov_b32_dpp v30, v29 row_mirror row_mask:0xf bank_mask:0xf
	s_waitcnt lgkmcnt(0)
	v_add_f32_e32 v29, v29, v30
	s_nop 1
	v_mov_b32_dpp v30, v29 row_half_mirror row_mask:0xf bank_mask:0xf
	s_waitcnt lgkmcnt(0)
	v_add_f32_e32 v29, v29, v30
	s_nop 1
	v_mov_b32_dpp v31, v29 quad_perm:[2,3,0,1] row_mask:0xf bank_mask:0xf
	v_or_b32_e32 v30, s6, v94
	v_mad_i64_i32 v[40:41], s[2:3], v30, s14, 0
	v_lshl_add_u64 v[40:41], v[40:41], 2, v[26:27]
	s_waitcnt lgkmcnt(0)
	v_add_f32_e32 v29, v29, v31
	s_nop 1
	v_mov_b32_dpp v39, v29 quad_perm:[1,0,3,2] row_mask:0xf bank_mask:0xf
	s_waitcnt vmcnt(5)
	v_sub_u32_e32 v31, v38, v37
	v_cmp_gt_u32_e64 s[2:3], 8, v31
	global_store_dwordx4 v[40:41], v[18:21], off
	global_store_dwordx4 v[40:41], v[22:25], off offset:16
	s_and_saveexec_b64 s[22:23], s[2:3]
	s_cbranch_execz .LBB10_15
	v_cmp_eq_u32_e64 s[2:3], v38, v37
	s_ashr_i32 s7, s6, 31
	s_nop 0
	v_cndmask_b32_e64 v18, 0, v18, s[2:3]
	v_cmp_eq_u32_e64 s[2:3], 4, v31
	s_nop 1
	v_cndmask_b32_e64 v18, v18, v22, s[2:3]
	v_cmp_eq_u32_e64 s[2:3], 1, v31
	s_nop 1
	v_cndmask_b32_e64 v18, v18, v19, s[2:3]
	v_cmp_eq_u32_e64 s[2:3], 5, v31
	s_nop 1
	v_cndmask_b32_e64 v18, v18, v23, s[2:3]
	v_cmp_eq_u32_e64 s[2:3], 2, v31
	s_nop 1
	v_cndmask_b32_e64 v18, v18, v20, s[2:3]
	v_cmp_eq_u32_e64 s[2:3], 6, v31
	s_nop 1
	v_cndmask_b32_e64 v18, v18, v24, s[2:3]
	v_cmp_eq_u32_e64 s[2:3], 3, v31
	s_nop 1
	v_cndmask_b32_e64 v18, v18, v21, s[2:3]
	v_cmp_eq_u32_e64 s[2:3], 7, v31
	s_nop 1
	v_cndmask_b32_e64 v20, v18, v25, s[2:3]
	v_lshl_add_u64 v[18:19], v[66:67], 0, s[6:7]
	v_lshl_add_u64 v[18:19], v[18:19], 2, s[24:25]
	global_store_dword v[18:19], v20, off offset:256

.LBB10_17:
	s_or_b64 exec, exec, s[2:3]
	v_add_u32_e32 v18, 0, v99
	ds_read_b128 v[18:21], v18
	v_add_u32_e32 v22, s5, v99
	v_add_u32_e32 v28, 0, v100
	ds_read_b128 v[22:25], v22
	ds_read_b128 v[28:31], v28
	ds_read_b64 v[42:43], v101
	v_add_u32_e32 v38, s5, v100
	s_waitcnt lgkmcnt(4)
	ds_read_b128 v[38:41], v38
	s_waitcnt lgkmcnt(3)
	v_pk_add_f32 v[18:19], v[18:19], v[22:23]
	v_pk_add_f32 v[20:21], v[20:21], v[24:25]
	s_waitcnt lgkmcnt(1)
	v_pk_fma_f32 v[6:7], v[42:43], v[6:7], v[18:19] op_sel_hi:[0,1,1] neg_lo:[1,0,0] neg_hi:[1,0,0]
	v_pk_fma_f32 v[6:7], v[42:43], v[6:7], v[14:15] op_sel:[1,0,0]
	s_waitcnt lgkmcnt(0)
	v_pk_add_f32 v[14:15], v[30:31], v[40:41]
	v_pk_add_f32 v[18:19], v[28:29], v[38:39]
	v_pk_fma_f32 v[4:5], v[42:43], v[4:5], v[14:15] op_sel_hi:[0,1,1] neg_lo:[1,0,0] neg_hi:[1,0,0]
	v_pk_fma_f32 v[2:3], v[42:43], v[2:3], v[18:19] op_sel_hi:[0,1,1] neg_lo:[1,0,0] neg_hi:[1,0,0]
	v_pk_fma_f32 v[8:9], v[42:43], v[8:9], v[20:21] op_sel_hi:[0,1,1] neg_lo:[1,0,0] neg_hi:[1,0,0]
	v_pk_fma_f32 v[4:5], v[42:43], v[4:5], v[12:13] op_sel:[1,0,0]
	v_pk_fma_f32 v[2:3], v[42:43], v[2:3], v[10:11] op_sel:[1,0,0]
	v_pk_fma_f32 v[8:9], v[42:43], v[8:9], v[16:17] op_sel:[1,0,0]
	v_max_f32_e32 v12, v4, v5
	v_max_f32_e32 v10, v6, v7
	v_max_f32_e32 v11, v8, v9
	v_max3_f32 v12, v2, v3, v12
	v_max3_f32 v10, v10, v11, v12
	s_nop 1
	v_mov_b32_dpp v11, v10 row_mirror row_mask:0xf bank_mask:0xf
	s_waitcnt lgkmcnt(0)
	v_max_f32_e32 v11, v11, v11
	v_max_f32_e32 v10, v10, v11
	s_nop 1
	v_mov_b32_dpp v11, v10 row_half_mirror row_mask:0xf bank_mask:0xf
	s_waitcnt lgkmcnt(0)
	v_max_f32_e32 v11, v11, v11
	v_max_f32_e32 v10, v10, v11
	s_nop 1
	v_mov_b32_dpp v11, v10 quad_perm:[2,3,0,1] row_mask:0xf bank_mask:0xf
	s_waitcnt lgkmcnt(0)
	v_max_f32_e32 v11, v11, v11
	v_max_f32_e32 v10, v10, v11
	s_nop 1
	v_mov_b32_dpp v11, v10 quad_perm:[1,0,3,2] row_mask:0xf bank_mask:0xf
	s_waitcnt lgkmcnt(0)
	v_max_f32_e32 v11, v11, v11
	v_max_f32_e32 v10, v10, v11
	v_sub_f32_e32 v11, v6, v10
	v_sub_f32_e32 v12, v2, v10
	v_sub_f32_e32 v13, v7, v10
	v_sub_f32_e32 v14, v3, v10
	v_mul_f32_e32 v11, 0x3fb8aa3b, v11
	v_mul_f32_e32 v12, 0x3fb8aa3b, v12
	v_mul_f32_e32 v13, 0x3fb8aa3b, v13
	v_mul_f32_e32 v14, 0x3fb8aa3b, v14
	v_exp_f32_e32 v11, v11
	v_exp_f32_e32 v12, v12
	v_exp_f32_e32 v13, v13
	v_exp_f32_e32 v14, v14
	v_sub_f32_e32 v15, v9, v10
	v_add_f32_e32 v11, v11, v12
	v_sub_f32_e32 v16, v5, v10
	v_add_f32_e32 v12, v13, v14
	v_sub_f32_e32 v13, v8, v10
	v_sub_f32_e32 v14, v4, v10
	v_mul_f32_e32 v13, 0x3fb8aa3b, v13
	v_mul_f32_e32 v14, 0x3fb8aa3b, v14
	v_exp_f32_e32 v13, v13
	v_exp_f32_e32 v14, v14
	v_mul_f32_e32 v15, 0x3fb8aa3b, v15
	v_mul_f32_e32 v16, 0x3fb8aa3b, v16
	v_exp_f32_e32 v15, v15
	v_exp_f32_e32 v16, v16
	v_add_f32_e32 v11, 0, v11
	v_add_f32_e32 v11, v11, v12
	v_add_f32_e32 v12, v13, v14
	v_add_f32_e32 v11, v11, v12
	v_add_f32_e32 v12, v15, v16
	v_add_f32_e32 v11, v11, v12
	s_nop 1
	v_mov_b32_dpp v12, v11 row_mirror row_mask:0xf bank_mask:0xf
	s_waitcnt lgkmcnt(0)
	v_add_f32_e32 v11, v11, v12
	s_nop 1
	v_mov_b32_dpp v12, v11 row_half_mirror row_mask:0xf bank_mask:0xf
	s_waitcnt lgkmcnt(0)
	v_add_f32_e32 v11, v11, v12
	s_nop 1
	v_mov_b32_dpp v13, v11 quad_perm:[2,3,0,1] row_mask:0xf bank_mask:0xf
	v_add_u32_e32 v12, s6, v98
	v_mad_i64_i32 v[14:15], s[2:3], v12, s14, 0
	v_lshl_add_u64 v[16:17], v[14:15], 2, v[26:27]
	s_waitcnt lgkmcnt(0)
	v_add_f32_e32 v11, v11, v13
	s_nop 1
	v_mov_b32_dpp v14, v11 quad_perm:[1,0,3,2] row_mask:0xf bank_mask:0xf
	s_waitcnt vmcnt(6)
	v_sub_u32_e32 v13, v32, v37
	v_cmp_gt_u32_e64 s[2:3], 8, v13
	global_store_dwordx4 v[16:17], v[6:9], off
	global_store_dwordx4 v[16:17], v[2:5], off offset:16
	s_and_saveexec_b64 s[22:23], s[2:3]
	s_cbranch_execz .LBB10_19
	v_cmp_eq_u32_e64 s[2:3], v32, v37
	s_ashr_i32 s7, s6, 31
	s_nop 0
	v_cndmask_b32_e64 v6, 0, v6, s[2:3]
	v_cmp_eq_u32_e64 s[2:3], 4, v13
	s_nop 1
	v_cndmask_b32_e64 v2, v6, v2, s[2:3]
	v_cmp_eq_u32_e64 s[2:3], 1, v13
	s_nop 1
	v_cndmask_b32_e64 v2, v2, v7, s[2:3]
	v_cmp_eq_u32_e64 s[2:3], 5, v13
	s_nop 1
	v_cndmask_b32_e64 v2, v2, v3, s[2:3]
	v_cmp_eq_u32_e64 s[2:3], 2, v13
	s_nop 1
	v_cndmask_b32_e64 v2, v2, v8, s[2:3]
	v_cmp_eq_u32_e64 s[2:3], 6, v13
	s_nop 1
	v_cndmask_b32_e64 v2, v2, v4, s[2:3]
	v_cmp_eq_u32_e64 s[2:3], 3, v13
	s_nop 1
	v_cndmask_b32_e64 v2, v2, v9, s[2:3]
	v_cmp_eq_u32_e64 s[2:3], 7, v13
	s_nop 1
	v_cndmask_b32_e64 v4, v2, v5, s[2:3]
	v_lshl_add_u64 v[2:3], v[66:67], 0, s[6:7]
	v_lshl_add_u64 v[2:3], v[2:3], 2, s[24:25]
	global_store_dword v[2:3], v4, off offset:384

amdhsa.kernels:
  - .agpr_count:     0
    .args:
      - .actual_access:  read_only
        .address_space:  global
        .offset:         0
        .size:           8
        .value_kind:     global_buffer
      - .actual_access:  read_only
        .address_space:  global
        .offset:         8
        .size:           8
        .value_kind:     global_buffer
      - .actual_access:  read_only
        .address_space:  global
        .offset:         16
        .size:           8
        .value_kind:     global_buffer
      - .actual_access:  read_only
        .address_space:  global
        .offset:         24
        .size:           8
        .value_kind:     global_buffer
      - .actual_access:  write_only
        .address_space:  global
        .offset:         32
        .size:           8
        .value_kind:     global_buffer
      - .actual_access:  write_only
        .address_space:  global
        .offset:         40
        .size:           8
        .value_kind:     global_buffer
    .group_segment_fixed_size: 0
    .kernarg_segment_align: 8
    .kernarg_segment_size: 48
    .language:       OpenCL C
    .language_version:
      - 2
      - 0
    .max_flat_workgroup_size: 256
    .name:           _Z9fold_sumsPKfS0_S0_S0_PfS1_
    .private_segment_fixed_size: 0
    .sgpr_count:     15
    .sgpr_spill_count: 0
    .symbol:         _Z9fold_sumsPKfS0_S0_S0_PfS1_.kd
    .uniform_work_group_size: 1
    .uses_dynamic_stack: false
    .vgpr_count:     24
    .vgpr_spill_count: 0
    .wavefront_size: 64
  - .agpr_count:     0
    .args:
      - .offset:         0
        .size:           208
        .value_kind:     by_value
    .group_segment_fixed_size: 10496
    .kernarg_segment_align: 8
    .kernarg_segment_size: 208
    .language:       OpenCL C
    .language_version:
      - 2
      - 0
    .max_flat_workgroup_size: 256
    .name:           _Z15prologue_kernel12PrologueArgs
    .private_segment_fixed_size: 0
    .sgpr_count:     30
    .sgpr_spill_count: 0
    .symbol:         _Z15prologue_kernel12PrologueArgs.kd
    .uniform_work_group_size: 1
    .uses_dynamic_stack: false
    .vgpr_count:     35
    .vgpr_spill_count: 0
    .wavefront_size: 64
  - .agpr_count:     0
    .args:
      - .address_space:  global
        .offset:         0
        .size:           8
        .value_kind:     global_buffer
      - .address_space:  global
        .offset:         8
        .size:           8
        .value_kind:     global_buffer
      - .actual_access:  read_only
        .address_space:  global
        .offset:         16
        .size:           8
        .value_kind:     global_buffer
      - .actual_access:  read_only
        .address_space:  global
        .offset:         24
        .size:           8
        .value_kind:     global_buffer
      - .actual_access:  read_only
        .address_space:  global
        .offset:         32
        .size:           8
        .value_kind:     global_buffer
      - .actual_access:  write_only
        .address_space:  global
        .offset:         40
        .size:           8
        .value_kind:     global_buffer
      - .actual_access:  write_only
        .address_space:  global
        .offset:         48
        .size:           8
        .value_kind:     global_buffer
      - .offset:         56
        .size:           4
        .value_kind:     by_value
      - .offset:         60
        .size:           4
        .value_kind:     by_value
    .group_segment_fixed_size: 0
    .kernarg_segment_align: 8
    .kernarg_segment_size: 64
    .language:       OpenCL C
    .language_version:
      - 2
      - 0
    .max_flat_workgroup_size: 512
    .name:           _Z11attn_kernelPKDF16_PDF16_PKfS3_S3_PfS4_ii
    .private_segment_fixed_size: 0
    .sgpr_count:     34
    .sgpr_spill_count: 0
    .symbol:         _Z11attn_kernelPKDF16_PDF16_PKfS3_S3_PfS4_ii.kd
    .uniform_work_group_size: 1
    .uses_dynamic_stack: false
    .vgpr_count:     128
    .vgpr_spill_count: 0
    .wavefront_size: 64
  - .agpr_count:     0
    .args:
      - .actual_access:  read_only
        .address_space:  global
        .offset:         0
        .size:           8
        .value_kind:     global_buffer
      - .actual_access:  read_only
        .address_space:  global
        .offset:         8
        .size:           8
        .value_kind:     global_buffer
      - .actual_access:  write_only
        .address_space:  global
        .offset:         16
        .size:           8
        .value_kind:     global_buffer
    .group_segment_fixed_size: 64
    .kernarg_segment_align: 8
    .kernarg_segment_size: 24
    .language:       OpenCL C
    .language_version:
      - 2
      - 0
    .max_flat_workgroup_size: 1024
    .name:           _Z12loss_combinePKfS0_Pf
    .private_segment_fixed_size: 0
    .sgpr_count:     20
    .sgpr_spill_count: 0
    .symbol:         _Z12loss_combinePKfS0_Pf.kd
    .uniform_work_group_size: 1
    .uses_dynamic_stack: false
    .vgpr_count:     76
    .vgpr_spill_count: 0
    .wavefront_size: 64
  - .agpr_count:     0
    .args:
      - .actual_access:  read_only
        .address_space:  global
        .offset:         0
        .size:           8
        .value_kind:     global_buffer
      - .actual_access:  read_only
        .address_space:  global
        .offset:         8
        .size:           8
        .value_kind:     global_buffer
      - .actual_access:  write_only
        .address_space:  global
        .offset:         16
        .size:           8
        .value_kind:     global_buffer
    .group_segment_fixed_size: 16
    .kernarg_segment_align: 8
    .kernarg_segment_size: 24
    .language:       OpenCL C
    .language_version:
      - 2
      - 0
    .max_flat_workgroup_size: 256
    .name:           _Z9loss_rowsPKfPKiPf
    .private_segment_fixed_size: 0
    .sgpr_count:     18
    .sgpr_spill_count: 0
    .symbol:         _Z9loss_rowsPKfPKiPf.kd
    .uniform_work_group_size: 1
    .uses_dynamic_stack: false
    .vgpr_count:     28
    .vgpr_spill_count: 0
    .wavefront_size: 64
  - .agpr_count:     0
    .args:
      - .actual_access:  read_only
        .address_space:  global
        .offset:         0
        .size:           8
        .value_kind:     global_buffer
      - .actual_access:  write_only
        .address_space:  global
        .offset:         8
        .size:           8
        .value_kind:     global_buffer
    .group_segment_fixed_size: 16
    .kernarg_segment_align: 8
    .kernarg_segment_size: 16
    .language:       OpenCL C
    .language_version:
      - 2
      - 0
    .max_flat_workgroup_size: 256
    .name:           _Z10loss_finalPKfPf
    .private_segment_fixed_size: 0
    .sgpr_count:     10
    .sgpr_spill_count: 0
    .symbol:         _Z10loss_finalPKfPf.kd
    .uniform_work_group_size: 1
    .uses_dynamic_stack: false
    .vgpr_count:     6
    .vgpr_spill_count: 0
    .wavefront_size: 64
  - .agpr_count:     0
    .args:
      - .address_space:  global
        .offset:         0
        .size:           8
        .value_kind:     global_buffer
      - .address_space:  global
        .offset:         8
        .size:           8
        .value_kind:     global_buffer
      - .offset:         16
        .size:           4
        .value_kind:     by_value
      - .offset:         20
        .size:           4
        .value_kind:     by_value
      - .offset:         24
        .size:           4
        .value_kind:     by_value
      - .offset:         28
        .size:           4
        .value_kind:     by_value
      - .offset:         32
        .size:           4
        .value_kind:     by_value
      - .offset:         36
        .size:           4
        .value_kind:     by_value
      - .actual_access:  read_only
        .address_space:  global
        .offset:         40
        .size:           8
        .value_kind:     global_buffer
      - .actual_access:  read_only
        .address_space:  global
        .offset:         48
        .size:           8
        .value_kind:     global_buffer
      - .actual_access:  read_only
        .address_space:  global
        .offset:         56
        .size:           8
        .value_kind:     global_buffer
      - .actual_access:  read_only
        .address_space:  global
        .offset:         64
        .size:           8
        .value_kind:     global_buffer
      - .actual_access:  write_only
        .address_space:  global
        .offset:         72
        .size:           8
        .value_kind:     global_buffer
      - .offset:         80
        .size:           144
        .value_kind:     by_value
    .group_segment_fixed_size: 0
    .kernarg_segment_align: 8
    .kernarg_segment_size: 224
    .language:       OpenCL C
    .language_version:
      - 2
      - 0
    .max_flat_workgroup_size: 512
    .name:           _Z6gemm_qILi0ELi1EEvPKDF16_S1_iiiiiiPKfS3_S3_S3_PDF16_8ConvArgs
    .private_segment_fixed_size: 0
    .sgpr_count:     50
    .sgpr_spill_count: 0
    .symbol:         _Z6gemm_qILi0ELi1EEvPKDF16_S1_iiiiiiPKfS3_S3_S3_PDF16_8ConvArgs.kd
    .uniform_work_group_size: 1
    .uses_dynamic_stack: false
    .vgpr_count:     244
    .vgpr_spill_count: 0
    .wavefront_size: 64
  - .agpr_count:     0
    .args:
      - .actual_access:  read_only
        .address_space:  global
        .offset:         0
        .size:           8
        .value_kind:     global_buffer
      - .actual_access:  read_only
        .address_space:  global
        .offset:         8
        .size:           8
        .value_kind:     global_buffer
      - .offset:         16
        .size:           4
        .value_kind:     by_value
      - .offset:         20
        .size:           4
        .value_kind:     by_value
      - .offset:         24
        .size:           4
        .value_kind:     by_value
      - .offset:         28
        .size:           4
        .value_kind:     by_value
      - .offset:         32
        .size:           4
        .value_kind:     by_value
      - .offset:         36
        .size:           4
        .value_kind:     by_value
      - .actual_access:  read_only
        .address_space:  global
        .offset:         40
        .size:           8
        .value_kind:     global_buffer
      - .actual_access:  read_only
        .address_space:  global
        .offset:         48
        .size:           8
        .value_kind:     global_buffer
      - .actual_access:  read_only
        .address_space:  global
        .offset:         56
        .size:           8
        .value_kind:     global_buffer
      - .address_space:  global
        .offset:         64
        .size:           8
        .value_kind:     global_buffer
      - .address_space:  global
        .offset:         72
        .size:           8
        .value_kind:     global_buffer
      - .actual_access:  write_only
        .address_space:  global
        .offset:         80
        .size:           8
        .value_kind:     global_buffer
      - .actual_access:  read_only
        .address_space:  global
        .offset:         88
        .size:           8
        .value_kind:     global_buffer
      - .actual_access:  read_only
        .address_space:  global
        .offset:         96
        .size:           8
        .value_kind:     global_buffer
      - .offset:         104
        .size:           4
        .value_kind:     hidden_block_count_x
      - .offset:         108
        .size:           4
        .value_kind:     hidden_block_count_y
      - .offset:         112
        .size:           4
        .value_kind:     hidden_block_count_z
      - .offset:         116
        .size:           2
        .value_kind:     hidden_group_size_x
      - .offset:         118
        .size:           2
        .value_kind:     hidden_group_size_y
      - .offset:         120
        .size:           2
        .value_kind:     hidden_group_size_z
      - .offset:         122
        .size:           2
        .value_kind:     hidden_remainder_x
      - .offset:         124
        .size:           2
        .value_kind:     hidden_remainder_y
      - .offset:         126
        .size:           2
        .value_kind:     hidden_remainder_z
      - .offset:         144
        .size:           8
        .value_kind:     hidden_global_offset_x
      - .offset:         152
        .size:           8
        .value_kind:     hidden_global_offset_y
      - .offset:         160
        .size:           8
        .value_kind:     hidden_global_offset_z
      - .offset:         168
        .size:           2
        .value_kind:     hidden_grid_dims
      - .offset:         224
        .size:           4
        .value_kind:     hidden_dynamic_lds_size
    .group_segment_fixed_size: 0
    .kernarg_segment_align: 8
    .kernarg_segment_size: 360
    .language:       OpenCL C
    .language_version:
      - 2
      - 0
    .max_flat_workgroup_size: 512
    .name:           _Z6gemm_pILi2ELi8EEvPKDF16_S1_iiiiiiPKfS3_S3_PfPDF16_S4_S5_S4_
    .private_segment_fixed_size: 0
    .sgpr_count:     58
    .sgpr_spill_count: 0
    .symbol:         _Z6gemm_pILi2ELi8EEvPKDF16_S1_iiiiiiPKfS3_S3_PfPDF16_S4_S5_S4_.kd
    .uniform_work_group_size: 1
    .uses_dynamic_stack: false
    .vgpr_count:     192
    .vgpr_spill_count: 0
    .wavefront_size: 64
  - .agpr_count:     0
    .args:
      - .address_space:  global
        .offset:         0
        .size:           8
        .value_kind:     global_buffer
      - .address_space:  global
        .offset:         8
        .size:           8
        .value_kind:     global_buffer
      - .offset:         16
        .size:           4
        .value_kind:     by_value
      - .offset:         20
        .size:           4
        .value_kind:     by_value
      - .offset:         24
        .size:           4
        .value_kind:     by_value
      - .offset:         28
        .size:           4
        .value_kind:     by_value
      - .offset:         32
        .size:           4
        .value_kind:     by_value
      - .offset:         36
        .size:           4
        .value_kind:     by_value
      - .actual_access:  read_only
        .address_space:  global
        .offset:         40
        .size:           8
        .value_kind:     global_buffer
      - .actual_access:  read_only
        .address_space:  global
        .offset:         48
        .size:           8
        .value_kind:     global_buffer
      - .actual_access:  read_only
        .address_space:  global
        .offset:         56
        .size:           8
        .value_kind:     global_buffer
      - .actual_access:  read_only
        .address_space:  global
        .offset:         64
        .size:           8
        .value_kind:     global_buffer
      - .actual_access:  write_only
        .address_space:  global
        .offset:         72
        .size:           8
        .value_kind:     global_buffer
      - .offset:         80
        .size:           144
        .value_kind:     by_value
    .group_segment_fixed_size: 0
    .kernarg_segment_align: 8
    .kernarg_segment_size: 224
    .language:       OpenCL C
    .language_version:
      - 2
      - 0
    .max_flat_workgroup_size: 512
    .name:           _Z6gemm_qILi1ELi0EEvPKDF16_S1_iiiiiiPKfS3_S3_S3_PDF16_8ConvArgs
    .private_segment_fixed_size: 0
    .sgpr_count:     29
    .sgpr_spill_count: 0
    .symbol:         _Z6gemm_qILi1ELi0EEvPKDF16_S1_iiiiiiPKfS3_S3_S3_PDF16_8ConvArgs.kd
    .uniform_work_group_size: 1
    .uses_dynamic_stack: false
    .vgpr_count:     244
    .vgpr_spill_count: 0
    .wavefront_size: 64
  - .agpr_count:     0
    .args:
      - .actual_access:  read_only
        .address_space:  global
        .offset:         0
        .size:           8
        .value_kind:     global_buffer
      - .actual_access:  read_only
        .address_space:  global
        .offset:         8
        .size:           8
        .value_kind:     global_buffer
      - .offset:         16
        .size:           4
        .value_kind:     by_value
      - .offset:         20
        .size:           4
        .value_kind:     by_value
      - .offset:         24
        .size:           4
        .value_kind:     by_value
      - .offset:         28
        .size:           4
        .value_kind:     by_value
      - .offset:         32
        .size:           4
        .value_kind:     by_value
      - .offset:         36
        .size:           4
        .value_kind:     by_value
      - .actual_access:  read_only
        .address_space:  global
        .offset:         40
        .size:           8
        .value_kind:     global_buffer
      - .actual_access:  read_only
        .address_space:  global
        .offset:         48
        .size:           8
        .value_kind:     global_buffer
      - .actual_access:  read_only
        .address_space:  global
        .offset:         56
        .size:           8
        .value_kind:     global_buffer
      - .address_space:  global
        .offset:         64
        .size:           8
        .value_kind:     global_buffer
      - .address_space:  global
        .offset:         72
        .size:           8
        .value_kind:     global_buffer
      - .actual_access:  write_only
        .address_space:  global
        .offset:         80
        .size:           8
        .value_kind:     global_buffer
      - .actual_access:  read_only
        .address_space:  global
        .offset:         88
        .size:           8
        .value_kind:     global_buffer
      - .actual_access:  read_only
        .address_space:  global
        .offset:         96
        .size:           8
        .value_kind:     global_buffer
      - .offset:         104
        .size:           4
        .value_kind:     hidden_block_count_x
      - .offset:         108
        .size:           4
        .value_kind:     hidden_block_count_y
      - .offset:         112
        .size:           4
        .value_kind:     hidden_block_count_z
      - .offset:         116
        .size:           2
        .value_kind:     hidden_group_size_x
      - .offset:         118
        .size:           2
        .value_kind:     hidden_group_size_y
      - .offset:         120
        .size:           2
        .value_kind:     hidden_group_size_z
      - .offset:         122
        .size:           2
        .value_kind:     hidden_remainder_x
      - .offset:         124
        .size:           2
        .value_kind:     hidden_remainder_y
      - .offset:         126
        .size:           2
        .value_kind:     hidden_remainder_z
      - .offset:         144
        .size:           8
        .value_kind:     hidden_global_offset_x
      - .offset:         152
        .size:           8
        .value_kind:     hidden_global_offset_y
      - .offset:         160
        .size:           8
        .value_kind:     hidden_global_offset_z
      - .offset:         168
        .size:           2
        .value_kind:     hidden_grid_dims
      - .offset:         224
        .size:           4
        .value_kind:     hidden_dynamic_lds_size
    .group_segment_fixed_size: 0
    .kernarg_segment_align: 8
    .kernarg_segment_size: 360
    .language:       OpenCL C
    .language_version:
      - 2
      - 0
    .max_flat_workgroup_size: 512
    .name:           _Z6gemm_pILi2ELi32EEvPKDF16_S1_iiiiiiPKfS3_S3_PfPDF16_S4_S5_S4_
    .private_segment_fixed_size: 0
    .sgpr_count:     58
    .sgpr_spill_count: 0
    .symbol:         _Z6gemm_pILi2ELi32EEvPKDF16_S1_iiiiiiPKfS3_S3_PfPDF16_S4_S5_S4_.kd
    .uniform_work_group_size: 1
    .uses_dynamic_stack: false
    .vgpr_count:     192
    .vgpr_spill_count: 0
    .wavefront_size: 64
  - .agpr_count:     0
    .args:
      - .actual_access:  read_only
        .address_space:  global
        .offset:         0
        .size:           8
        .value_kind:     global_buffer
      - .actual_access:  read_only
        .address_space:  global
        .offset:         8
        .size:           8
        .value_kind:     global_buffer
      - .offset:         16
        .size:           4
        .value_kind:     by_value
      - .offset:         20
        .size:           4
        .value_kind:     by_value
      - .offset:         24
        .size:           4
        .value_kind:     by_value
      - .offset:         28
        .size:           4
        .value_kind:     by_value
      - .offset:         32
        .size:           4
        .value_kind:     by_value
      - .offset:         36
        .size:           4
        .value_kind:     by_value
      - .actual_access:  read_only
        .address_space:  global
        .offset:         40
        .size:           8
        .value_kind:     global_buffer
      - .actual_access:  read_only
        .address_space:  global
        .offset:         48
        .size:           8
        .value_kind:     global_buffer
      - .actual_access:  read_only
        .address_space:  global
        .offset:         56
        .size:           8
        .value_kind:     global_buffer
      - .address_space:  global
        .offset:         64
        .size:           8
        .value_kind:     global_buffer
      - .actual_access:  read_only
        .address_space:  global
        .offset:         72
        .size:           8
        .value_kind:     global_buffer
      - .actual_access:  write_only
        .address_space:  global
        .offset:         80
        .size:           8
        .value_kind:     global_buffer
      - .actual_access:  read_only
        .address_space:  global
        .offset:         88
        .size:           8
        .value_kind:     global_buffer
      - .actual_access:  write_only
        .address_space:  global
        .offset:         96
        .size:           8
        .value_kind:     global_buffer
      - .offset:         104
        .size:           4
        .value_kind:     hidden_block_count_x
      - .offset:         108
        .size:           4
        .value_kind:     hidden_block_count_y
      - .offset:         112
        .size:           4
        .value_kind:     hidden_block_count_z
      - .offset:         116
        .size:           2
        .value_kind:     hidden_group_size_x
      - .offset:         118
        .size:           2
        .value_kind:     hidden_group_size_y
      - .offset:         120
        .size:           2
        .value_kind:     hidden_group_size_z
      - .offset:         122
        .size:           2
        .value_kind:     hidden_remainder_x
      - .offset:         124
        .size:           2
        .value_kind:     hidden_remainder_y
      - .offset:         126
        .size:           2
        .value_kind:     hidden_remainder_z
      - .offset:         144
        .size:           8
        .value_kind:     hidden_global_offset_x
      - .offset:         152
        .size:           8
        .value_kind:     hidden_global_offset_y
      - .offset:         160
        .size:           8
        .value_kind:     hidden_global_offset_z
      - .offset:         168
        .size:           2
        .value_kind:     hidden_grid_dims
      - .offset:         224
        .size:           4
        .value_kind:     hidden_dynamic_lds_size
    .group_segment_fixed_size: 0
    .kernarg_segment_align: 8
    .kernarg_segment_size: 360
    .language:       OpenCL C
    .language_version:
      - 2
      - 0
    .max_flat_workgroup_size: 512
    .name:           _Z6gemm_pILi3ELi8EEvPKDF16_S1_iiiiiiPKfS3_S3_PfPDF16_S4_S5_S4_
    .private_segment_fixed_size: 0
    .sgpr_count:     46
    .sgpr_spill_count: 0
    .symbol:         _Z6gemm_pILi3ELi8EEvPKDF16_S1_iiiiiiPKfS3_S3_PfPDF16_S4_S5_S4_.kd
    .uniform_work_group_size: 1
    .uses_dynamic_stack: false
    .vgpr_count:     148
    .vgpr_spill_count: 0
    .wavefront_size: 64
